# v33 + hand-written down-GEMM EpiRes2 epilogue (row scale and residual loads issued up front, packed f32 fma, transposed coalesced stores)
# speedup vs baseline: 1.0085x; 1.0019x over previous
.LBB0_2036:
	s_add_u32 s4, s46, 0x1d70000
	s_addc_u32 s5, s47, 0
	s_lshl_b32 s6, s0, 8
	s_add_i32 s0, s6, s74
	s_lshl_b32 s7, s1, 5
	s_lshl_b32 s98, s10, 8
	s_or_b32 s7, s7, s98
	s_lshl_b32 s98, s1, 2
	v_lshl_add_u32 v249, v167, 4, s98
	v_or_b32_e32 v142, s0, v146
	v_lshrrev_b32_e32 v143, 1, v248
	v_and_or_b32 v143, v143, 24, s7
	v_mov_b32_e32 v246, v142
	v_mov_b32_e32 v247, 0
	v_lshl_add_u64 v[246:247], v[246:247], 4, s[4:5]
	v_lshlrev_b32_e32 v142, 11, v142
	v_lshl_add_u32 v142, v143, 1, v142
	v_mov_b32_e32 v143, 0
	v_lshl_add_u64 v[142:143], s[60:61], 0, v[142:143]
	s_mov_b32 s98, 0x8000
	s_mov_b32 s99, 0
	s_mov_b32 s100, 0x28000
	s_mov_b32 s101, 0
	global_load_dwordx4 v[214:217], v[246:247], off
	global_load_dwordx4 v[218:221], v[246:247], off offset:256
	global_load_dwordx4 v[222:225], v[246:247], off offset:512
	global_load_dwordx4 v[226:229], v[246:247], off offset:768
	global_load_dwordx4 v[230:233], v[246:247], off offset:2048
	global_load_dwordx4 v[234:237], v[246:247], off offset:2304
	global_load_dwordx4 v[238:241], v[246:247], off offset:2560
	global_load_dwordx4 v[242:245], v[246:247], off offset:2816
	global_load_dwordx4 v[150:153], v[142:143], off
	global_load_dwordx4 v[154:157], v[142:143], off offset:256
	v_lshl_add_u64 v[142:143], v[142:143], 0, s[98:99]
	global_load_dwordx4 v[158:161], v[142:143], off
	global_load_dwordx4 v[162:165], v[142:143], off offset:256
	v_lshl_add_u64 v[142:143], v[142:143], 0, s[98:99]
	global_load_dwordx4 v[166:169], v[142:143], off
	global_load_dwordx4 v[170:173], v[142:143], off offset:256
	v_lshl_add_u64 v[142:143], v[142:143], 0, s[98:99]
	global_load_dwordx4 v[174:177], v[142:143], off
	global_load_dwordx4 v[178:181], v[142:143], off offset:256
	v_lshl_add_u64 v[142:143], v[142:143], 0, s[100:101]
	global_load_dwordx4 v[182:185], v[142:143], off
	global_load_dwordx4 v[186:189], v[142:143], off offset:256
	v_lshl_add_u64 v[142:143], v[142:143], 0, s[98:99]
	global_load_dwordx4 v[190:193], v[142:143], off
	global_load_dwordx4 v[194:197], v[142:143], off offset:256
	v_lshl_add_u64 v[142:143], v[142:143], 0, s[98:99]
	global_load_dwordx4 v[198:201], v[142:143], off
	global_load_dwordx4 v[202:205], v[142:143], off offset:256
	v_lshl_add_u64 v[142:143], v[142:143], 0, s[98:99]
	global_load_dwordx4 v[206:209], v[142:143], off
	global_load_dwordx4 v[210:213], v[142:143], off offset:256
	v_lshrrev_b32_e32 v144, 2, v248
	v_and_b32_e32 v145, 3, v248
	v_lshlrev_b32_e32 v147, 6, v145
	v_lshl_add_u32 v147, v144, 2, v147
	v_add_u32_e32 v144, s0, v144
	v_lshl_or_b32 v145, v145, 3, s7
	v_lshlrev_b32_e32 v144, 11, v144
	v_lshl_add_u32 v144, v145, 1, v144
	v_mov_b32_e32 v145, 0
	v_lshl_add_u64 v[144:145], s[60:61], 0, v[144:145]
	v_xor_b32_e32 v148, 16, v248
	v_lshlrev_b32_e32 v148, 2, v148
	v_xor_b32_e32 v149, 32, v248
	v_lshlrev_b32_e32 v149, 2, v149
	v_mov_b32_e32 v250, 0x358637bd
	s_mov_b32 s7, 0xffff0000
	s_barrier
	s_waitcnt vmcnt(16)
	v_add_f32_e32 v214, v214, v215
	v_add_f32_e32 v216, v216, v217
	v_add_f32_e32 v218, v218, v219
	v_add_f32_e32 v220, v220, v221
	v_add_f32_e32 v222, v222, v223
	v_add_f32_e32 v224, v224, v225
	v_add_f32_e32 v226, v226, v227
	v_add_f32_e32 v228, v228, v229
	v_add_f32_e32 v230, v230, v231
	v_add_f32_e32 v232, v232, v233
	v_add_f32_e32 v234, v234, v235
	v_add_f32_e32 v236, v236, v237
	v_add_f32_e32 v238, v238, v239
	v_add_f32_e32 v240, v240, v241
	v_add_f32_e32 v242, v242, v243
	v_add_f32_e32 v244, v244, v245
	v_add_f32_e32 v214, v214, v216
	v_add_f32_e32 v218, v218, v220
	v_add_f32_e32 v222, v222, v224
	v_add_f32_e32 v226, v226, v228
	v_add_f32_e32 v230, v230, v232
	v_add_f32_e32 v234, v234, v236
	v_add_f32_e32 v238, v238, v240
	v_add_f32_e32 v242, v242, v244
	v_fmamk_f32 v214, v214, 0x3a800000, v250
	v_fmamk_f32 v218, v218, 0x3a800000, v250
	v_fmamk_f32 v222, v222, 0x3a800000, v250
	v_fmamk_f32 v226, v226, 0x3a800000, v250
	v_fmamk_f32 v230, v230, 0x3a800000, v250
	v_fmamk_f32 v234, v234, 0x3a800000, v250
	v_fmamk_f32 v238, v238, 0x3a800000, v250
	v_fmamk_f32 v242, v242, 0x3a800000, v250
	v_rcp_f32_e32 v214, v214
	v_rcp_f32_e32 v218, v218
	v_rcp_f32_e32 v222, v222
	v_rcp_f32_e32 v226, v226
	v_rcp_f32_e32 v230, v230
	v_rcp_f32_e32 v234, v234
	v_rcp_f32_e32 v238, v238
	v_rcp_f32_e32 v242, v242
	s_nop 0
	s_waitcnt vmcnt(15)
	v_lshlrev_b32_e32 v134, 16, v150
	v_and_b32_e32 v135, s7, v150
	v_lshlrev_b32_e32 v136, 16, v151
	v_and_b32_e32 v137, s7, v151
	v_lshlrev_b32_e32 v138, 16, v152
	v_and_b32_e32 v139, s7, v152
	v_lshlrev_b32_e32 v140, 16, v153
	v_and_b32_e32 v141, s7, v153
	v_pk_fma_f32 v[130:131], v[130:131], v[214:215], v[134:135] op_sel_hi:[1,0,1]
	v_pk_fma_f32 v[132:133], v[132:133], v[214:215], v[136:137] op_sel_hi:[1,0,1]
	v_pk_fma_f32 v[126:127], v[126:127], v[214:215], v[138:139] op_sel_hi:[1,0,1]
	v_pk_fma_f32 v[128:129], v[128:129], v[214:215], v[140:141] op_sel_hi:[1,0,1]
	v_pk_mul_f32 v[216:217], v[130:131], v[130:131]
	v_pk_fma_f32 v[216:217], v[132:133], v[132:133], v[216:217]
	v_pk_fma_f32 v[216:217], v[126:127], v[126:127], v[216:217]
	v_pk_fma_f32 v[216:217], v[128:129], v[128:129], v[216:217]
	v_cvt_pk_bf16_f32 v130, v130, v131
	v_cvt_pk_bf16_f32 v131, v132, v133
	v_cvt_pk_bf16_f32 v132, v126, v127
	v_cvt_pk_bf16_f32 v133, v128, v129
	ds_bpermute_b32 v130, v147, v130
	ds_bpermute_b32 v131, v147, v131
	ds_bpermute_b32 v132, v147, v132
	ds_bpermute_b32 v133, v147, v133
	s_waitcnt vmcnt(14)
	v_lshlrev_b32_e32 v134, 16, v154
	v_and_b32_e32 v135, s7, v154
	v_lshlrev_b32_e32 v136, 16, v155
	v_and_b32_e32 v137, s7, v155
	v_lshlrev_b32_e32 v138, 16, v156
	v_and_b32_e32 v139, s7, v156
	v_lshlrev_b32_e32 v140, 16, v157
	v_and_b32_e32 v141, s7, v157
	v_pk_fma_f32 v[122:123], v[122:123], v[214:215], v[134:135] op_sel_hi:[1,0,1]
	v_pk_fma_f32 v[124:125], v[124:125], v[214:215], v[136:137] op_sel_hi:[1,0,1]
	v_pk_fma_f32 v[118:119], v[118:119], v[214:215], v[138:139] op_sel_hi:[1,0,1]
	v_pk_fma_f32 v[120:121], v[120:121], v[214:215], v[140:141] op_sel_hi:[1,0,1]
	v_pk_fma_f32 v[216:217], v[122:123], v[122:123], v[216:217]
	v_pk_fma_f32 v[216:217], v[124:125], v[124:125], v[216:217]
	v_pk_fma_f32 v[216:217], v[118:119], v[118:119], v[216:217]
	v_pk_fma_f32 v[216:217], v[120:121], v[120:121], v[216:217]
	v_add_f32_e32 v215, v216, v217
	v_cvt_pk_bf16_f32 v122, v122, v123
	v_cvt_pk_bf16_f32 v123, v124, v125
	v_cvt_pk_bf16_f32 v124, v118, v119
	v_cvt_pk_bf16_f32 v125, v120, v121
	ds_bpermute_b32 v122, v147, v122
	ds_bpermute_b32 v123, v147, v123
	ds_bpermute_b32 v124, v147, v124
	ds_bpermute_b32 v125, v147, v125
	s_waitcnt lgkmcnt(4)
	global_store_dwordx4 v[144:145], v[130:133], off
	s_waitcnt vmcnt(14)
	v_lshlrev_b32_e32 v134, 16, v158
	v_and_b32_e32 v135, s7, v158
	v_lshlrev_b32_e32 v136, 16, v159
	v_and_b32_e32 v137, s7, v159
	v_lshlrev_b32_e32 v138, 16, v160
	v_and_b32_e32 v139, s7, v160
	v_lshlrev_b32_e32 v140, 16, v161
	v_and_b32_e32 v141, s7, v161
	v_pk_fma_f32 v[114:115], v[114:115], v[218:219], v[134:135] op_sel_hi:[1,0,1]
	v_pk_fma_f32 v[116:117], v[116:117], v[218:219], v[136:137] op_sel_hi:[1,0,1]
	v_pk_fma_f32 v[106:107], v[106:107], v[218:219], v[138:139] op_sel_hi:[1,0,1]
	v_pk_fma_f32 v[108:109], v[108:109], v[218:219], v[140:141] op_sel_hi:[1,0,1]
	v_pk_mul_f32 v[220:221], v[114:115], v[114:115]
	v_pk_fma_f32 v[220:221], v[116:117], v[116:117], v[220:221]
	v_pk_fma_f32 v[220:221], v[106:107], v[106:107], v[220:221]
	v_pk_fma_f32 v[220:221], v[108:109], v[108:109], v[220:221]
	v_cvt_pk_bf16_f32 v114, v114, v115
	v_cvt_pk_bf16_f32 v115, v116, v117
	v_cvt_pk_bf16_f32 v116, v106, v107
	v_cvt_pk_bf16_f32 v117, v108, v109
	ds_bpermute_b32 v114, v147, v114
	ds_bpermute_b32 v115, v147, v115
	ds_bpermute_b32 v116, v147, v116
	ds_bpermute_b32 v117, v147, v117
	s_waitcnt lgkmcnt(4)
	global_store_dwordx4 v[144:145], v[122:125], off offset:256
	v_lshl_add_u64 v[144:145], v[144:145], 0, s[98:99]
	s_waitcnt vmcnt(14)
	v_lshlrev_b32_e32 v134, 16, v162
	v_and_b32_e32 v135, s7, v162
	v_lshlrev_b32_e32 v136, 16, v163
	v_and_b32_e32 v137, s7, v163
	v_lshlrev_b32_e32 v138, 16, v164
	v_and_b32_e32 v139, s7, v164
	v_lshlrev_b32_e32 v140, 16, v165
	v_and_b32_e32 v141, s7, v165
	v_pk_fma_f32 v[102:103], v[102:103], v[218:219], v[134:135] op_sel_hi:[1,0,1]
	v_pk_fma_f32 v[104:105], v[104:105], v[218:219], v[136:137] op_sel_hi:[1,0,1]
	v_pk_fma_f32 v[98:99], v[98:99], v[218:219], v[138:139] op_sel_hi:[1,0,1]
	v_pk_fma_f32 v[100:101], v[100:101], v[218:219], v[140:141] op_sel_hi:[1,0,1]
	v_pk_fma_f32 v[220:221], v[102:103], v[102:103], v[220:221]
	v_pk_fma_f32 v[220:221], v[104:105], v[104:105], v[220:221]
	v_pk_fma_f32 v[220:221], v[98:99], v[98:99], v[220:221]
	v_pk_fma_f32 v[220:221], v[100:101], v[100:101], v[220:221]
	v_add_f32_e32 v219, v220, v221
	v_cvt_pk_bf16_f32 v102, v102, v103
	v_cvt_pk_bf16_f32 v103, v104, v105
	v_cvt_pk_bf16_f32 v104, v98, v99
	v_cvt_pk_bf16_f32 v105, v100, v101
	ds_bpermute_b32 v102, v147, v102
	ds_bpermute_b32 v103, v147, v103
	ds_bpermute_b32 v104, v147, v104
	ds_bpermute_b32 v105, v147, v105
	s_waitcnt lgkmcnt(4)
	global_store_dwordx4 v[144:145], v[114:117], off
	s_waitcnt vmcnt(14)
	v_lshlrev_b32_e32 v134, 16, v166
	v_and_b32_e32 v135, s7, v166
	v_lshlrev_b32_e32 v136, 16, v167
	v_and_b32_e32 v137, s7, v167
	v_lshlrev_b32_e32 v138, 16, v168
	v_and_b32_e32 v139, s7, v168
	v_lshlrev_b32_e32 v140, 16, v169
	v_and_b32_e32 v141, s7, v169
	v_pk_fma_f32 v[94:95], v[94:95], v[222:223], v[134:135] op_sel_hi:[1,0,1]
	v_pk_fma_f32 v[96:97], v[96:97], v[222:223], v[136:137] op_sel_hi:[1,0,1]
	v_pk_fma_f32 v[90:91], v[90:91], v[222:223], v[138:139] op_sel_hi:[1,0,1]
	v_pk_fma_f32 v[92:93], v[92:93], v[222:223], v[140:141] op_sel_hi:[1,0,1]
	v_pk_mul_f32 v[224:225], v[94:95], v[94:95]
	v_pk_fma_f32 v[224:225], v[96:97], v[96:97], v[224:225]
	v_pk_fma_f32 v[224:225], v[90:91], v[90:91], v[224:225]
	v_pk_fma_f32 v[224:225], v[92:93], v[92:93], v[224:225]
	v_cvt_pk_bf16_f32 v94, v94, v95
	v_cvt_pk_bf16_f32 v95, v96, v97
	v_cvt_pk_bf16_f32 v96, v90, v91
	v_cvt_pk_bf16_f32 v97, v92, v93
	ds_bpermute_b32 v94, v147, v94
	ds_bpermute_b32 v95, v147, v95
	ds_bpermute_b32 v96, v147, v96
	ds_bpermute_b32 v97, v147, v97
	s_waitcnt lgkmcnt(4)
	global_store_dwordx4 v[144:145], v[102:105], off offset:256
	v_lshl_add_u64 v[144:145], v[144:145], 0, s[98:99]
	s_waitcnt vmcnt(14)
	v_lshlrev_b32_e32 v134, 16, v170
	v_and_b32_e32 v135, s7, v170
	v_lshlrev_b32_e32 v136, 16, v171
	v_and_b32_e32 v137, s7, v171
	v_lshlrev_b32_e32 v138, 16, v172
	v_and_b32_e32 v139, s7, v172
	v_lshlrev_b32_e32 v140, 16, v173
	v_and_b32_e32 v141, s7, v173
	v_pk_fma_f32 v[86:87], v[86:87], v[222:223], v[134:135] op_sel_hi:[1,0,1]
	v_pk_fma_f32 v[88:89], v[88:89], v[222:223], v[136:137] op_sel_hi:[1,0,1]
	v_pk_fma_f32 v[82:83], v[82:83], v[222:223], v[138:139] op_sel_hi:[1,0,1]
	v_pk_fma_f32 v[84:85], v[84:85], v[222:223], v[140:141] op_sel_hi:[1,0,1]
	v_pk_fma_f32 v[224:225], v[86:87], v[86:87], v[224:225]
	v_pk_fma_f32 v[224:225], v[88:89], v[88:89], v[224:225]
	v_pk_fma_f32 v[224:225], v[82:83], v[82:83], v[224:225]
	v_pk_fma_f32 v[224:225], v[84:85], v[84:85], v[224:225]
	v_add_f32_e32 v223, v224, v225
	v_cvt_pk_bf16_f32 v86, v86, v87
	v_cvt_pk_bf16_f32 v87, v88, v89
	v_cvt_pk_bf16_f32 v88, v82, v83
	v_cvt_pk_bf16_f32 v89, v84, v85
	ds_bpermute_b32 v86, v147, v86
	ds_bpermute_b32 v87, v147, v87
	ds_bpermute_b32 v88, v147, v88
	ds_bpermute_b32 v89, v147, v89
	s_waitcnt lgkmcnt(4)
	global_store_dwordx4 v[144:145], v[94:97], off
	s_waitcnt vmcnt(14)
	v_lshlrev_b32_e32 v134, 16, v174
	v_and_b32_e32 v135, s7, v174
	v_lshlrev_b32_e32 v136, 16, v175
	v_and_b32_e32 v137, s7, v175
	v_lshlrev_b32_e32 v138, 16, v176
	v_and_b32_e32 v139, s7, v176
	v_lshlrev_b32_e32 v140, 16, v177
	v_and_b32_e32 v141, s7, v177
	v_pk_fma_f32 v[78:79], v[78:79], v[226:227], v[134:135] op_sel_hi:[1,0,1]
	v_pk_fma_f32 v[80:81], v[80:81], v[226:227], v[136:137] op_sel_hi:[1,0,1]
	v_pk_fma_f32 v[74:75], v[74:75], v[226:227], v[138:139] op_sel_hi:[1,0,1]
	v_pk_fma_f32 v[76:77], v[76:77], v[226:227], v[140:141] op_sel_hi:[1,0,1]
	v_pk_mul_f32 v[228:229], v[78:79], v[78:79]
	v_pk_fma_f32 v[228:229], v[80:81], v[80:81], v[228:229]
	v_pk_fma_f32 v[228:229], v[74:75], v[74:75], v[228:229]
	v_pk_fma_f32 v[228:229], v[76:77], v[76:77], v[228:229]
	v_cvt_pk_bf16_f32 v78, v78, v79
	v_cvt_pk_bf16_f32 v79, v80, v81
	v_cvt_pk_bf16_f32 v80, v74, v75
	v_cvt_pk_bf16_f32 v81, v76, v77
	ds_bpermute_b32 v78, v147, v78
	ds_bpermute_b32 v79, v147, v79
	ds_bpermute_b32 v80, v147, v80
	ds_bpermute_b32 v81, v147, v81
	s_waitcnt lgkmcnt(4)
	global_store_dwordx4 v[144:145], v[86:89], off offset:256
	v_lshl_add_u64 v[144:145], v[144:145], 0, s[98:99]
	s_waitcnt vmcnt(14)
	v_lshlrev_b32_e32 v134, 16, v178
	v_and_b32_e32 v135, s7, v178
	v_lshlrev_b32_e32 v136, 16, v179
	v_and_b32_e32 v137, s7, v179
	v_lshlrev_b32_e32 v138, 16, v180
	v_and_b32_e32 v139, s7, v180
	v_lshlrev_b32_e32 v140, 16, v181
	v_and_b32_e32 v141, s7, v181
	v_pk_fma_f32 v[70:71], v[70:71], v[226:227], v[134:135] op_sel_hi:[1,0,1]
	v_pk_fma_f32 v[72:73], v[72:73], v[226:227], v[136:137] op_sel_hi:[1,0,1]
	v_pk_fma_f32 v[66:67], v[66:67], v[226:227], v[138:139] op_sel_hi:[1,0,1]
	v_pk_fma_f32 v[68:69], v[68:69], v[226:227], v[140:141] op_sel_hi:[1,0,1]
	v_pk_fma_f32 v[228:229], v[70:71], v[70:71], v[228:229]
	v_pk_fma_f32 v[228:229], v[72:73], v[72:73], v[228:229]
	v_pk_fma_f32 v[228:229], v[66:67], v[66:67], v[228:229]
	v_pk_fma_f32 v[228:229], v[68:69], v[68:69], v[228:229]
	v_add_f32_e32 v227, v228, v229
	v_cvt_pk_bf16_f32 v70, v70, v71
	v_cvt_pk_bf16_f32 v71, v72, v73
	v_cvt_pk_bf16_f32 v72, v66, v67
	v_cvt_pk_bf16_f32 v73, v68, v69
	ds_bpermute_b32 v70, v147, v70
	ds_bpermute_b32 v71, v147, v71
	ds_bpermute_b32 v72, v147, v72
	ds_bpermute_b32 v73, v147, v73
	s_waitcnt lgkmcnt(4)
	global_store_dwordx4 v[144:145], v[78:81], off
	s_waitcnt vmcnt(14)
	v_lshlrev_b32_e32 v134, 16, v182
	v_and_b32_e32 v135, s7, v182
	v_lshlrev_b32_e32 v136, 16, v183
	v_and_b32_e32 v137, s7, v183
	v_lshlrev_b32_e32 v138, 16, v184
	v_and_b32_e32 v139, s7, v184
	v_lshlrev_b32_e32 v140, 16, v185
	v_and_b32_e32 v141, s7, v185
	v_pk_fma_f32 v[62:63], v[62:63], v[230:231], v[134:135] op_sel_hi:[1,0,1]
	v_pk_fma_f32 v[64:65], v[64:65], v[230:231], v[136:137] op_sel_hi:[1,0,1]
	v_pk_fma_f32 v[58:59], v[58:59], v[230:231], v[138:139] op_sel_hi:[1,0,1]
	v_pk_fma_f32 v[60:61], v[60:61], v[230:231], v[140:141] op_sel_hi:[1,0,1]
	v_pk_mul_f32 v[232:233], v[62:63], v[62:63]
	v_pk_fma_f32 v[232:233], v[64:65], v[64:65], v[232:233]
	v_pk_fma_f32 v[232:233], v[58:59], v[58:59], v[232:233]
	v_pk_fma_f32 v[232:233], v[60:61], v[60:61], v[232:233]
	v_cvt_pk_bf16_f32 v62, v62, v63
	v_cvt_pk_bf16_f32 v63, v64, v65
	v_cvt_pk_bf16_f32 v64, v58, v59
	v_cvt_pk_bf16_f32 v65, v60, v61
	ds_bpermute_b32 v62, v147, v62
	ds_bpermute_b32 v63, v147, v63
	ds_bpermute_b32 v64, v147, v64
	ds_bpermute_b32 v65, v147, v65
	s_waitcnt lgkmcnt(4)
	global_store_dwordx4 v[144:145], v[70:73], off offset:256
	v_lshl_add_u64 v[144:145], v[144:145], 0, s[100:101]
	s_waitcnt vmcnt(14)
	v_lshlrev_b32_e32 v134, 16, v186
	v_and_b32_e32 v135, s7, v186
	v_lshlrev_b32_e32 v136, 16, v187
	v_and_b32_e32 v137, s7, v187
	v_lshlrev_b32_e32 v138, 16, v188
	v_and_b32_e32 v139, s7, v188
	v_lshlrev_b32_e32 v140, 16, v189
	v_and_b32_e32 v141, s7, v189
	v_pk_fma_f32 v[54:55], v[54:55], v[230:231], v[134:135] op_sel_hi:[1,0,1]
	v_pk_fma_f32 v[56:57], v[56:57], v[230:231], v[136:137] op_sel_hi:[1,0,1]
	v_pk_fma_f32 v[50:51], v[50:51], v[230:231], v[138:139] op_sel_hi:[1,0,1]
	v_pk_fma_f32 v[52:53], v[52:53], v[230:231], v[140:141] op_sel_hi:[1,0,1]
	v_pk_fma_f32 v[232:233], v[54:55], v[54:55], v[232:233]
	v_pk_fma_f32 v[232:233], v[56:57], v[56:57], v[232:233]
	v_pk_fma_f32 v[232:233], v[50:51], v[50:51], v[232:233]
	v_pk_fma_f32 v[232:233], v[52:53], v[52:53], v[232:233]
	v_add_f32_e32 v231, v232, v233
	v_cvt_pk_bf16_f32 v54, v54, v55
	v_cvt_pk_bf16_f32 v55, v56, v57
	v_cvt_pk_bf16_f32 v56, v50, v51
	v_cvt_pk_bf16_f32 v57, v52, v53
	ds_bpermute_b32 v54, v147, v54
	ds_bpermute_b32 v55, v147, v55
	ds_bpermute_b32 v56, v147, v56
	ds_bpermute_b32 v57, v147, v57
	s_waitcnt lgkmcnt(4)
	global_store_dwordx4 v[144:145], v[62:65], off
	s_waitcnt vmcnt(14)
	v_lshlrev_b32_e32 v134, 16, v190
	v_and_b32_e32 v135, s7, v190
	v_lshlrev_b32_e32 v136, 16, v191
	v_and_b32_e32 v137, s7, v191
	v_lshlrev_b32_e32 v138, 16, v192
	v_and_b32_e32 v139, s7, v192
	v_lshlrev_b32_e32 v140, 16, v193
	v_and_b32_e32 v141, s7, v193
	v_pk_fma_f32 v[46:47], v[46:47], v[234:235], v[134:135] op_sel_hi:[1,0,1]
	v_pk_fma_f32 v[48:49], v[48:49], v[234:235], v[136:137] op_sel_hi:[1,0,1]
	v_pk_fma_f32 v[42:43], v[42:43], v[234:235], v[138:139] op_sel_hi:[1,0,1]
	v_pk_fma_f32 v[44:45], v[44:45], v[234:235], v[140:141] op_sel_hi:[1,0,1]
	v_pk_mul_f32 v[236:237], v[46:47], v[46:47]
	v_pk_fma_f32 v[236:237], v[48:49], v[48:49], v[236:237]
	v_pk_fma_f32 v[236:237], v[42:43], v[42:43], v[236:237]
	v_pk_fma_f32 v[236:237], v[44:45], v[44:45], v[236:237]
	v_cvt_pk_bf16_f32 v46, v46, v47
	v_cvt_pk_bf16_f32 v47, v48, v49
	v_cvt_pk_bf16_f32 v48, v42, v43
	v_cvt_pk_bf16_f32 v49, v44, v45
	ds_bpermute_b32 v46, v147, v46
	ds_bpermute_b32 v47, v147, v47
	ds_bpermute_b32 v48, v147, v48
	ds_bpermute_b32 v49, v147, v49
	s_waitcnt lgkmcnt(4)
	global_store_dwordx4 v[144:145], v[54:57], off offset:256
	v_lshl_add_u64 v[144:145], v[144:145], 0, s[98:99]
	s_waitcnt vmcnt(14)
	v_lshlrev_b32_e32 v134, 16, v194
	v_and_b32_e32 v135, s7, v194
	v_lshlrev_b32_e32 v136, 16, v195
	v_and_b32_e32 v137, s7, v195
	v_lshlrev_b32_e32 v138, 16, v196
	v_and_b32_e32 v139, s7, v196
	v_lshlrev_b32_e32 v140, 16, v197
	v_and_b32_e32 v141, s7, v197
	v_pk_fma_f32 v[38:39], v[38:39], v[234:235], v[134:135] op_sel_hi:[1,0,1]
	v_pk_fma_f32 v[40:41], v[40:41], v[234:235], v[136:137] op_sel_hi:[1,0,1]
	v_pk_fma_f32 v[34:35], v[34:35], v[234:235], v[138:139] op_sel_hi:[1,0,1]
	v_pk_fma_f32 v[36:37], v[36:37], v[234:235], v[140:141] op_sel_hi:[1,0,1]
	v_pk_fma_f32 v[236:237], v[38:39], v[38:39], v[236:237]
	v_pk_fma_f32 v[236:237], v[40:41], v[40:41], v[236:237]
	v_pk_fma_f32 v[236:237], v[34:35], v[34:35], v[236:237]
	v_pk_fma_f32 v[236:237], v[36:37], v[36:37], v[236:237]
	v_add_f32_e32 v235, v236, v237
	v_cvt_pk_bf16_f32 v38, v38, v39
	v_cvt_pk_bf16_f32 v39, v40, v41
	v_cvt_pk_bf16_f32 v40, v34, v35
	v_cvt_pk_bf16_f32 v41, v36, v37
	ds_bpermute_b32 v38, v147, v38
	ds_bpermute_b32 v39, v147, v39
	ds_bpermute_b32 v40, v147, v40
	ds_bpermute_b32 v41, v147, v41
	s_waitcnt lgkmcnt(4)
	global_store_dwordx4 v[144:145], v[46:49], off
	s_waitcnt vmcnt(14)
	v_lshlrev_b32_e32 v134, 16, v198
	v_and_b32_e32 v135, s7, v198
	v_lshlrev_b32_e32 v136, 16, v199
	v_and_b32_e32 v137, s7, v199
	v_lshlrev_b32_e32 v138, 16, v200
	v_and_b32_e32 v139, s7, v200
	v_lshlrev_b32_e32 v140, 16, v201
	v_and_b32_e32 v141, s7, v201
	v_pk_fma_f32 v[30:31], v[30:31], v[238:239], v[134:135] op_sel_hi:[1,0,1]
	v_pk_fma_f32 v[32:33], v[32:33], v[238:239], v[136:137] op_sel_hi:[1,0,1]
	v_pk_fma_f32 v[26:27], v[26:27], v[238:239], v[138:139] op_sel_hi:[1,0,1]
	v_pk_fma_f32 v[28:29], v[28:29], v[238:239], v[140:141] op_sel_hi:[1,0,1]
	v_pk_mul_f32 v[240:241], v[30:31], v[30:31]
	v_pk_fma_f32 v[240:241], v[32:33], v[32:33], v[240:241]
	v_pk_fma_f32 v[240:241], v[26:27], v[26:27], v[240:241]
	v_pk_fma_f32 v[240:241], v[28:29], v[28:29], v[240:241]
	v_cvt_pk_bf16_f32 v30, v30, v31
	v_cvt_pk_bf16_f32 v31, v32, v33
	v_cvt_pk_bf16_f32 v32, v26, v27
	v_cvt_pk_bf16_f32 v33, v28, v29
	ds_bpermute_b32 v30, v147, v30
	ds_bpermute_b32 v31, v147, v31
	ds_bpermute_b32 v32, v147, v32
	ds_bpermute_b32 v33, v147, v33
	s_waitcnt lgkmcnt(4)
	global_store_dwordx4 v[144:145], v[38:41], off offset:256
	v_lshl_add_u64 v[144:145], v[144:145], 0, s[98:99]
	s_waitcnt vmcnt(14)
	v_lshlrev_b32_e32 v134, 16, v202
	v_and_b32_e32 v135, s7, v202
	v_lshlrev_b32_e32 v136, 16, v203
	v_and_b32_e32 v137, s7, v203
	v_lshlrev_b32_e32 v138, 16, v204
	v_and_b32_e32 v139, s7, v204
	v_lshlrev_b32_e32 v140, 16, v205
	v_and_b32_e32 v141, s7, v205
	v_pk_fma_f32 v[22:23], v[22:23], v[238:239], v[134:135] op_sel_hi:[1,0,1]
	v_pk_fma_f32 v[24:25], v[24:25], v[238:239], v[136:137] op_sel_hi:[1,0,1]
	v_pk_fma_f32 v[18:19], v[18:19], v[238:239], v[138:139] op_sel_hi:[1,0,1]
	v_pk_fma_f32 v[20:21], v[20:21], v[238:239], v[140:141] op_sel_hi:[1,0,1]
	v_pk_fma_f32 v[240:241], v[22:23], v[22:23], v[240:241]
	v_pk_fma_f32 v[240:241], v[24:25], v[24:25], v[240:241]
	v_pk_fma_f32 v[240:241], v[18:19], v[18:19], v[240:241]
	v_pk_fma_f32 v[240:241], v[20:21], v[20:21], v[240:241]
	v_add_f32_e32 v239, v240, v241
	v_cvt_pk_bf16_f32 v22, v22, v23
	v_cvt_pk_bf16_f32 v23, v24, v25
	v_cvt_pk_bf16_f32 v24, v18, v19
	v_cvt_pk_bf16_f32 v25, v20, v21
	ds_bpermute_b32 v22, v147, v22
	ds_bpermute_b32 v23, v147, v23
	ds_bpermute_b32 v24, v147, v24
	ds_bpermute_b32 v25, v147, v25
	s_waitcnt lgkmcnt(4)
	global_store_dwordx4 v[144:145], v[30:33], off
	s_waitcnt vmcnt(14)
	v_lshlrev_b32_e32 v134, 16, v206
	v_and_b32_e32 v135, s7, v206
	v_lshlrev_b32_e32 v136, 16, v207
	v_and_b32_e32 v137, s7, v207
	v_lshlrev_b32_e32 v138, 16, v208
	v_and_b32_e32 v139, s7, v208
	v_lshlrev_b32_e32 v140, 16, v209
	v_and_b32_e32 v141, s7, v209
	v_pk_fma_f32 v[14:15], v[14:15], v[242:243], v[134:135] op_sel_hi:[1,0,1]
	v_pk_fma_f32 v[16:17], v[16:17], v[242:243], v[136:137] op_sel_hi:[1,0,1]
	v_pk_fma_f32 v[10:11], v[10:11], v[242:243], v[138:139] op_sel_hi:[1,0,1]
	v_pk_fma_f32 v[12:13], v[12:13], v[242:243], v[140:141] op_sel_hi:[1,0,1]
	v_pk_mul_f32 v[244:245], v[14:15], v[14:15]
	v_pk_fma_f32 v[244:245], v[16:17], v[16:17], v[244:245]
	v_pk_fma_f32 v[244:245], v[10:11], v[10:11], v[244:245]
	v_pk_fma_f32 v[244:245], v[12:13], v[12:13], v[244:245]
	v_cvt_pk_bf16_f32 v14, v14, v15
	v_cvt_pk_bf16_f32 v15, v16, v17
	v_cvt_pk_bf16_f32 v16, v10, v11
	v_cvt_pk_bf16_f32 v17, v12, v13
	ds_bpermute_b32 v14, v147, v14
	ds_bpermute_b32 v15, v147, v15
	ds_bpermute_b32 v16, v147, v16
	ds_bpermute_b32 v17, v147, v17
	s_waitcnt lgkmcnt(4)
	global_store_dwordx4 v[144:145], v[22:25], off offset:256
	v_lshl_add_u64 v[144:145], v[144:145], 0, s[98:99]
	s_waitcnt vmcnt(14)
	v_lshlrev_b32_e32 v134, 16, v210
	v_and_b32_e32 v135, s7, v210
	v_lshlrev_b32_e32 v136, 16, v211
	v_and_b32_e32 v137, s7, v211
	v_lshlrev_b32_e32 v138, 16, v212
	v_and_b32_e32 v139, s7, v212
	v_lshlrev_b32_e32 v140, 16, v213
	v_and_b32_e32 v141, s7, v213
	v_pk_fma_f32 v[6:7], v[6:7], v[242:243], v[134:135] op_sel_hi:[1,0,1]
	v_pk_fma_f32 v[8:9], v[8:9], v[242:243], v[136:137] op_sel_hi:[1,0,1]
	v_pk_fma_f32 v[2:3], v[2:3], v[242:243], v[138:139] op_sel_hi:[1,0,1]
	v_pk_fma_f32 v[4:5], v[4:5], v[242:243], v[140:141] op_sel_hi:[1,0,1]
	v_pk_fma_f32 v[244:245], v[6:7], v[6:7], v[244:245]
	v_pk_fma_f32 v[244:245], v[8:9], v[8:9], v[244:245]
	v_pk_fma_f32 v[244:245], v[2:3], v[2:3], v[244:245]
	v_pk_fma_f32 v[244:245], v[4:5], v[4:5], v[244:245]
	v_add_f32_e32 v243, v244, v245
	v_cvt_pk_bf16_f32 v6, v6, v7
	v_cvt_pk_bf16_f32 v7, v8, v9
	v_cvt_pk_bf16_f32 v8, v2, v3
	v_cvt_pk_bf16_f32 v9, v4, v5
	ds_bpermute_b32 v6, v147, v6
	ds_bpermute_b32 v7, v147, v7
	ds_bpermute_b32 v8, v147, v8
	ds_bpermute_b32 v9, v147, v9
	s_waitcnt lgkmcnt(4)
	global_store_dwordx4 v[144:145], v[14:17], off
	s_waitcnt lgkmcnt(0)
	global_store_dwordx4 v[144:145], v[6:9], off offset:256
	ds_bpermute_b32 v150, v148, v215
	ds_bpermute_b32 v151, v148, v219
	ds_bpermute_b32 v152, v148, v223
	ds_bpermute_b32 v153, v148, v227
	ds_bpermute_b32 v154, v148, v231
	ds_bpermute_b32 v155, v148, v235
	ds_bpermute_b32 v156, v148, v239
	ds_bpermute_b32 v157, v148, v243
	s_waitcnt lgkmcnt(0)
	v_add_f32_e32 v215, v215, v150
	v_add_f32_e32 v219, v219, v151
	v_add_f32_e32 v223, v223, v152
	v_add_f32_e32 v227, v227, v153
	v_add_f32_e32 v231, v231, v154
	v_add_f32_e32 v235, v235, v155
	v_add_f32_e32 v239, v239, v156
	v_add_f32_e32 v243, v243, v157
	ds_bpermute_b32 v150, v149, v215
	ds_bpermute_b32 v151, v149, v219
	ds_bpermute_b32 v152, v149, v223
	ds_bpermute_b32 v153, v149, v227
	ds_bpermute_b32 v154, v149, v231
	ds_bpermute_b32 v155, v149, v235
	ds_bpermute_b32 v156, v149, v239
	ds_bpermute_b32 v157, v149, v243
	s_waitcnt lgkmcnt(0)
	v_add_f32_e32 v215, v215, v150
	v_add_f32_e32 v219, v219, v151
	v_add_f32_e32 v223, v223, v152
	v_add_f32_e32 v227, v227, v153
	v_add_f32_e32 v231, v231, v154
	v_add_f32_e32 v235, v235, v155
	v_add_f32_e32 v239, v239, v156
	v_add_f32_e32 v243, v243, v157
	v_cmp_gt_u32_e32 vcc, 16, v248
	s_and_saveexec_b64 s[0:1], vcc
	ds_write_b32 v249, v215
	ds_write_b32 v249, v219 offset:256
	ds_write_b32 v249, v223 offset:512
	ds_write_b32 v249, v227 offset:768
	ds_write_b32 v249, v231 offset:2048
	ds_write_b32 v249, v235 offset:2304
	ds_write_b32 v249, v239 offset:2560
	ds_write_b32 v249, v243 offset:2816
	s_or_b64 exec, exec, s[0:1]
	s_waitcnt lgkmcnt(0)
	s_barrier
	s_andn2_b32 s49, s49, 63
	v_or_b32_e32 v1, s49, v248
	s_movk_i32 s0, 0x100
	v_cmp_gt_i32_e32 vcc, s0, v1
	s_and_saveexec_b64 s[0:1], vcc
	s_cbranch_execz .LBB0_2054
	v_lshl_add_u32 v2, v1, 4, 0
	s_waitcnt lgkmcnt(0)
	ds_read_b128 v[2:5], v2
	v_add_u32_e32 v6, s6, v1
	v_ashrrev_i32_e32 v7, 31, v6
	s_ashr_i32 s11, s10, 31
	s_waitcnt lgkmcnt(0)
	v_mov_b32_e32 v8, v3
	v_mov_b32_e32 v9, v4
	v_mov_b32_e32 v3, v5
	v_pk_add_f32 v[2:3], v[8:9], v[2:3]
	s_nop 0
	v_add_f32_e32 v1, v2, v3
	v_lshl_add_u64 v[2:3], v[6:7], 4, s[46:47]
	v_lshl_add_u64 v[2:3], s[10:11], 2, v[2:3]
	v_add_co_u32_e32 v2, vcc, 0x1db0000, v2
	s_nop 1
	v_addc_co_u32_e32 v3, vcc, 0, v3, vcc
	global_store_dword v[2:3], v1, off
